# slow path reuses the masks computed by the fast prologue (no re-classification); granule publish; pipelined refine
# speedup vs baseline: 1.0230x; 1.0025x over previous
.Lrg_slow:
	s_getpc_b64 s[4:5]
	s_and_b32 s4, s4, -16
	v_lshlrev_b32_e32 v2, 4, v1
	global_load_dwordx4 v[100:103], v2, s[4:5] offset:0
	global_load_dwordx4 v[104:107], v2, s[4:5] offset:1024
	global_load_dwordx4 v[108:111], v2, s[4:5] offset:2048
	global_load_dwordx4 v[112:115], v2, s[4:5] offset:3072
	s_add_u32 s4, s4, 0x1000
	s_addc_u32 s5, s5, 0
	global_load_dwordx4 v[116:119], v2, s[4:5] offset:0
	global_load_dwordx4 v[120:123], v2, s[4:5] offset:1024
	global_load_dwordx4 v[124:127], v2, s[4:5] offset:2048
	global_load_dwordx4 v[128:131], v2, s[4:5] offset:3072
	s_add_u32 s4, s4, 0x1000
	s_addc_u32 s5, s5, 0
	global_load_dwordx4 v[100:103], v2, s[4:5] offset:0
	global_load_dwordx4 v[104:107], v2, s[4:5] offset:1024
	global_load_dwordx4 v[108:111], v2, s[4:5] offset:2048
	global_load_dwordx4 v[112:115], v2, s[4:5] offset:3072
	s_add_u32 s4, s4, 0x1000
	s_addc_u32 s5, s5, 0
	global_load_dwordx4 v[116:119], v2, s[4:5] offset:0
	global_load_dwordx4 v[120:123], v2, s[4:5] offset:1024
	global_load_dwordx4 v[124:127], v2, s[4:5] offset:2048
	global_load_dwordx4 v[128:131], v2, s[4:5] offset:3072
	s_add_u32 s4, s4, 0x1000
	s_addc_u32 s5, s5, 0
	s_mov_b32 s3, s24
	s_mov_b32 s33, s27
	v_mov_b32_e32 v26, v1
	v_cmp_gt_u32_e64 s[10:11], 64, v0
	v_mov_b32_e32 v2, s50
	v_mov_b32_e32 v3, s51
	v_mov_b32_e32 v4, s54
	v_mov_b32_e32 v5, s55
	v_mov_b32_e32 v1, 0
	v_cmp_eq_u32_e32 vcc, 0, v0
	s_and_saveexec_b64 s[6:7], vcc
	ds_write_b128 v1, v[2:5] offset:16400
